# out-proj GEMM epilogue: all 16 residual tile loads issued up front into dead fragment VGPRs, one wait instead of 16 serialized round trips
# speedup vs baseline: 1.0167x; 1.0167x over previous
.LBB0_2136:
	s_add_u32 s18, s16, 0x100
	s_addc_u32 s19, s17, 0
	s_add_i32 s46, 0, 0x10000
	v_add_u32_e32 v2, s46, v149
	ds_read_b128 v[144:147], v2
	ds_read_b128 v[152:155], v2 offset:1024
	ds_read_b128 v[156:159], v2 offset:2048
	ds_read_b128 v[160:163], v2 offset:3072
	s_cmp_eq_u32 s45, 12
	s_cselect_b32 s23, s11, s19
	s_cselect_b32 s22, s10, s18
	s_cselect_b32 s21, s15, s44
	s_cselect_b32 s20, s14, s7
	v_lshl_add_u64 v[196:197], s[16:17], 0, v[140:141]
	s_add_i32 m0, s30, 0xc000
	ds_read_b128 v[164:167], v150
	ds_read_b128 v[168:171], v150 offset:1024
	ds_read_b128 v[172:175], v150 offset:2048
	ds_read_b128 v[176:179], v150 offset:3072
	ds_read_b128 v[180:183], v150 offset:4096
	ds_read_b128 v[184:187], v150 offset:5120
	ds_read_b128 v[188:191], v150 offset:6144
	ds_read_b128 v[192:195], v150 offset:7168
	global_load_lds_dwordx4 v[196:197], off
	v_lshl_add_u64 v[196:197], s[16:17], 0, v[142:143]
	s_add_i32 m0, s30, 0xe000
	s_nop 0
	global_load_lds_dwordx4 v[196:197], off
	s_waitcnt lgkmcnt(8)
	s_barrier
	s_waitcnt lgkmcnt(0)
	s_setprio 1
	s_waitcnt lgkmcnt(0)
	v_mfma_f32_16x16x32_bf16 v[128:131], v[144:147], v[164:167], v[128:131]
	v_mfma_f32_16x16x32_bf16 v[124:127], v[156:159], v[164:167], v[124:127]
	v_mfma_f32_16x16x32_bf16 v[112:115], v[144:147], v[172:175], v[112:115]
	v_mfma_f32_16x16x32_bf16 v[108:111], v[156:159], v[172:175], v[108:111]
	v_mfma_f32_16x16x32_bf16 v[96:99], v[144:147], v[180:183], v[96:99]
	v_mfma_f32_16x16x32_bf16 v[92:95], v[156:159], v[180:183], v[92:95]
	v_mfma_f32_16x16x32_bf16 v[80:83], v[144:147], v[188:191], v[80:83]
	v_mfma_f32_16x16x32_bf16 v[76:79], v[156:159], v[188:191], v[76:79]
	v_mfma_f32_16x16x32_bf16 v[128:131], v[152:155], v[168:171], v[128:131]
	v_mfma_f32_16x16x32_bf16 v[124:127], v[160:163], v[168:171], v[124:127]
	v_mfma_f32_16x16x32_bf16 v[112:115], v[152:155], v[176:179], v[112:115]
	v_mfma_f32_16x16x32_bf16 v[108:111], v[160:163], v[176:179], v[108:111]
	v_mfma_f32_16x16x32_bf16 v[96:99], v[152:155], v[184:187], v[96:99]
	v_mfma_f32_16x16x32_bf16 v[92:95], v[160:163], v[184:187], v[92:95]
	v_mfma_f32_16x16x32_bf16 v[80:83], v[152:155], v[192:195], v[80:83]
	v_mfma_f32_16x16x32_bf16 v[76:79], v[160:163], v[192:195], v[76:79]
	s_setprio 0
	s_barrier
	s_add_i32 s47, 0, 0x14000
	s_add_i32 s16, s46, s29
	v_add_u32_e32 v2, s47, v149
	v_lshl_add_u64 v[212:213], s[20:21], 0, v[136:137]
	s_mov_b32 m0, s16
	ds_read_b128 v[196:199], v2
	ds_read_b128 v[200:203], v2 offset:1024
	ds_read_b128 v[204:207], v2 offset:2048
	ds_read_b128 v[208:211], v2 offset:3072
	global_load_lds_dwordx4 v[212:213], off
	v_lshl_add_u64 v[222:223], s[20:21], 0, v[132:133]
	s_add_i32 m0, s16, 0x2000
	s_nop 0
	global_load_lds_dwordx4 v[222:223], off
	s_barrier
	s_waitcnt lgkmcnt(0)
	s_setprio 1
	s_waitcnt lgkmcnt(0)
	v_mfma_f32_16x16x32_bf16 v[120:123], v[196:199], v[164:167], v[120:123]
	v_mfma_f32_16x16x32_bf16 v[116:119], v[204:207], v[164:167], v[116:119]
	v_mfma_f32_16x16x32_bf16 v[104:107], v[196:199], v[172:175], v[104:107]
	v_mfma_f32_16x16x32_bf16 v[100:103], v[204:207], v[172:175], v[100:103]
	v_mfma_f32_16x16x32_bf16 v[88:91], v[196:199], v[180:183], v[88:91]
	v_mfma_f32_16x16x32_bf16 v[84:87], v[204:207], v[180:183], v[84:87]
	v_mfma_f32_16x16x32_bf16 v[72:75], v[196:199], v[188:191], v[72:75]
	v_mfma_f32_16x16x32_bf16 v[68:71], v[204:207], v[188:191], v[68:71]
	v_mfma_f32_16x16x32_bf16 v[120:123], v[200:203], v[168:171], v[120:123]
	v_mfma_f32_16x16x32_bf16 v[116:119], v[208:211], v[168:171], v[116:119]
	v_mfma_f32_16x16x32_bf16 v[104:107], v[200:203], v[176:179], v[104:107]
	v_mfma_f32_16x16x32_bf16 v[100:103], v[208:211], v[176:179], v[100:103]
	v_mfma_f32_16x16x32_bf16 v[88:91], v[200:203], v[184:187], v[88:91]
	v_mfma_f32_16x16x32_bf16 v[84:87], v[208:211], v[184:187], v[84:87]
	v_mfma_f32_16x16x32_bf16 v[72:75], v[200:203], v[192:195], v[72:75]
	v_mfma_f32_16x16x32_bf16 v[68:71], v[208:211], v[192:195], v[68:71]
	s_setprio 0
	s_mov_b32 m0, s30
	v_lshl_add_u64 v[224:225], s[22:23], 0, v[138:139]
	s_barrier
	ds_read_b128 v[164:167], v150 offset:16384
	ds_read_b128 v[168:171], v150 offset:17408
	ds_read_b128 v[172:175], v150 offset:18432
	ds_read_b128 v[176:179], v150 offset:19456
	ds_read_b128 v[180:183], v150 offset:20480
	ds_read_b128 v[184:187], v150 offset:21504
	ds_read_b128 v[188:191], v150 offset:22528
	ds_read_b128 v[192:195], v150 offset:23552
	global_load_lds_dwordx4 v[224:225], off
	v_lshl_add_u64 v[230:231], s[22:23], 0, v[134:135]
	s_mov_b32 m0, s31
	s_nop 0
	global_load_lds_dwordx4 v[230:231], off
	s_barrier
	s_waitcnt lgkmcnt(0)
	s_setprio 1
	s_waitcnt lgkmcnt(0)
	v_mfma_f32_16x16x32_bf16 v[64:67], v[144:147], v[164:167], v[64:67]
	v_mfma_f32_16x16x32_bf16 v[60:63], v[156:159], v[164:167], v[60:63]
	v_mfma_f32_16x16x32_bf16 v[48:51], v[144:147], v[172:175], v[48:51]
	v_mfma_f32_16x16x32_bf16 v[44:47], v[156:159], v[172:175], v[44:47]
	v_mfma_f32_16x16x32_bf16 v[32:35], v[144:147], v[180:183], v[32:35]
	v_mfma_f32_16x16x32_bf16 v[28:31], v[156:159], v[180:183], v[28:31]
	v_mfma_f32_16x16x32_bf16 v[16:19], v[144:147], v[188:191], v[16:19]
	v_mfma_f32_16x16x32_bf16 v[12:15], v[156:159], v[188:191], v[12:15]
	v_mfma_f32_16x16x32_bf16 v[64:67], v[152:155], v[168:171], v[64:67]
	v_mfma_f32_16x16x32_bf16 v[60:63], v[160:163], v[168:171], v[60:63]
	v_mfma_f32_16x16x32_bf16 v[48:51], v[152:155], v[176:179], v[48:51]
	v_mfma_f32_16x16x32_bf16 v[44:47], v[160:163], v[176:179], v[44:47]
	v_mfma_f32_16x16x32_bf16 v[32:35], v[152:155], v[184:187], v[32:35]
	v_mfma_f32_16x16x32_bf16 v[28:31], v[160:163], v[184:187], v[28:31]
	v_mfma_f32_16x16x32_bf16 v[16:19], v[152:155], v[192:195], v[16:19]
	v_mfma_f32_16x16x32_bf16 v[12:15], v[160:163], v[192:195], v[12:15]
	s_setprio 0
	s_barrier
	s_add_u32 s16, s20, 0x40000
	s_addc_u32 s17, s21, 0
	s_add_i32 s46, s47, s29
	v_lshl_add_u64 v[144:145], s[16:17], 0, v[136:137]
	s_mov_b32 m0, s46
	s_nop 0
	global_load_lds_dwordx4 v[144:145], off
	v_lshl_add_u64 v[144:145], s[16:17], 0, v[132:133]
	s_add_i32 m0, s46, 0x2000
	s_nop 0
	global_load_lds_dwordx4 v[144:145], off
	s_waitcnt vmcnt(6)
	s_barrier
	s_setprio 1
	v_mfma_f32_16x16x32_bf16 v[56:59], v[196:199], v[164:167], v[56:59]
	v_mfma_f32_16x16x32_bf16 v[52:55], v[204:207], v[164:167], v[52:55]
	v_mfma_f32_16x16x32_bf16 v[40:43], v[196:199], v[172:175], v[40:43]
	v_mfma_f32_16x16x32_bf16 v[36:39], v[204:207], v[172:175], v[36:39]
	v_mfma_f32_16x16x32_bf16 v[24:27], v[196:199], v[180:183], v[24:27]
	v_mfma_f32_16x16x32_bf16 v[20:23], v[204:207], v[180:183], v[20:23]
	v_mfma_f32_16x16x32_bf16 v[8:11], v[196:199], v[188:191], v[8:11]
	v_mfma_f32_16x16x32_bf16 v[4:7], v[204:207], v[188:191], v[4:7]
	v_mfma_f32_16x16x32_bf16 v[56:59], v[200:203], v[168:171], v[56:59]
	v_mfma_f32_16x16x32_bf16 v[52:55], v[208:211], v[168:171], v[52:55]
	v_mfma_f32_16x16x32_bf16 v[40:43], v[200:203], v[176:179], v[40:43]
	v_mfma_f32_16x16x32_bf16 v[36:39], v[208:211], v[176:179], v[36:39]
	v_mfma_f32_16x16x32_bf16 v[24:27], v[200:203], v[184:187], v[24:27]
	v_mfma_f32_16x16x32_bf16 v[20:23], v[208:211], v[184:187], v[20:23]
	v_mfma_f32_16x16x32_bf16 v[8:11], v[200:203], v[192:195], v[8:11]
	v_mfma_f32_16x16x32_bf16 v[4:7], v[208:211], v[192:195], v[4:7]
	s_setprio 0
	s_add_i32 s46, 0, 0x18000
	v_add_u32_e32 v2, s46, v149
	s_barrier
	ds_read_b128 v[144:147], v2
	ds_read_b128 v[152:155], v2 offset:1024
	ds_read_b128 v[156:159], v2 offset:2048
	ds_read_b128 v[160:163], v2 offset:3072
	s_add_u32 s16, s22, 0x120000
	s_addc_u32 s17, s23, 0
	s_mov_b32 m0, s34
	v_lshl_add_u64 v[196:197], s[16:17], 0, v[138:139]
	ds_read_b128 v[164:167], v150 offset:32768
	ds_read_b128 v[168:171], v150 offset:33792
	ds_read_b128 v[172:175], v150 offset:34816
	ds_read_b128 v[176:179], v150 offset:35840
	ds_read_b128 v[180:183], v150 offset:36864
	ds_read_b128 v[184:187], v150 offset:37888
	ds_read_b128 v[188:191], v150 offset:38912
	ds_read_b128 v[192:195], v150 offset:39936
	global_load_lds_dwordx4 v[196:197], off
	v_lshl_add_u64 v[196:197], s[16:17], 0, v[134:135]
	s_mov_b32 m0, s35
	s_nop 0
	global_load_lds_dwordx4 v[196:197], off
	s_waitcnt lgkmcnt(8)
	s_barrier
	s_waitcnt lgkmcnt(0)
	s_setprio 1
	s_waitcnt lgkmcnt(0)
	v_mfma_f32_16x16x32_bf16 v[128:131], v[144:147], v[164:167], v[128:131]
	v_mfma_f32_16x16x32_bf16 v[124:127], v[156:159], v[164:167], v[124:127]
	v_mfma_f32_16x16x32_bf16 v[112:115], v[144:147], v[172:175], v[112:115]
	v_mfma_f32_16x16x32_bf16 v[108:111], v[156:159], v[172:175], v[108:111]
	v_mfma_f32_16x16x32_bf16 v[96:99], v[144:147], v[180:183], v[96:99]
	v_mfma_f32_16x16x32_bf16 v[92:95], v[156:159], v[180:183], v[92:95]
	v_mfma_f32_16x16x32_bf16 v[80:83], v[144:147], v[188:191], v[80:83]
	v_mfma_f32_16x16x32_bf16 v[76:79], v[156:159], v[188:191], v[76:79]
	v_mfma_f32_16x16x32_bf16 v[128:131], v[152:155], v[168:171], v[128:131]
	v_mfma_f32_16x16x32_bf16 v[124:127], v[160:163], v[168:171], v[124:127]
	v_mfma_f32_16x16x32_bf16 v[112:115], v[152:155], v[176:179], v[112:115]
	v_mfma_f32_16x16x32_bf16 v[108:111], v[160:163], v[176:179], v[108:111]
	v_mfma_f32_16x16x32_bf16 v[96:99], v[152:155], v[184:187], v[96:99]
	v_mfma_f32_16x16x32_bf16 v[92:95], v[160:163], v[184:187], v[92:95]
	v_mfma_f32_16x16x32_bf16 v[80:83], v[152:155], v[192:195], v[80:83]
	v_mfma_f32_16x16x32_bf16 v[76:79], v[160:163], v[192:195], v[76:79]
	s_setprio 0
	s_barrier
	s_add_i32 s22, 0, 0x1c000
	s_add_i32 s16, s46, s29
	v_add_u32_e32 v2, s22, v149
	v_lshl_add_u64 v[212:213], v[212:213], 0, s[60:61]
	s_mov_b32 m0, s16
	ds_read_b128 v[196:199], v2
	ds_read_b128 v[200:203], v2 offset:1024
	ds_read_b128 v[204:207], v2 offset:2048
	ds_read_b128 v[208:211], v2 offset:3072
	global_load_lds_dwordx4 v[212:213], off
	v_lshl_add_u64 v[212:213], v[222:223], 0, s[60:61]
	s_add_i32 m0, s16, 0x2000
	s_nop 0
	global_load_lds_dwordx4 v[212:213], off
	s_barrier
	s_waitcnt lgkmcnt(0)
	s_setprio 1
	s_waitcnt lgkmcnt(0)
	v_mfma_f32_16x16x32_bf16 v[120:123], v[196:199], v[164:167], v[120:123]
	v_mfma_f32_16x16x32_bf16 v[116:119], v[204:207], v[164:167], v[116:119]
	v_mfma_f32_16x16x32_bf16 v[104:107], v[196:199], v[172:175], v[104:107]
	v_mfma_f32_16x16x32_bf16 v[100:103], v[204:207], v[172:175], v[100:103]
	v_mfma_f32_16x16x32_bf16 v[88:91], v[196:199], v[180:183], v[88:91]
	v_mfma_f32_16x16x32_bf16 v[84:87], v[204:207], v[180:183], v[84:87]
	v_mfma_f32_16x16x32_bf16 v[72:75], v[196:199], v[188:191], v[72:75]
	v_mfma_f32_16x16x32_bf16 v[68:71], v[204:207], v[188:191], v[68:71]
	v_mfma_f32_16x16x32_bf16 v[120:123], v[200:203], v[168:171], v[120:123]
	v_mfma_f32_16x16x32_bf16 v[116:119], v[208:211], v[168:171], v[116:119]
	v_mfma_f32_16x16x32_bf16 v[104:107], v[200:203], v[176:179], v[104:107]
	v_mfma_f32_16x16x32_bf16 v[100:103], v[208:211], v[176:179], v[100:103]
	v_mfma_f32_16x16x32_bf16 v[88:91], v[200:203], v[184:187], v[88:91]
	v_mfma_f32_16x16x32_bf16 v[84:87], v[208:211], v[184:187], v[84:87]
	v_mfma_f32_16x16x32_bf16 v[72:75], v[200:203], v[192:195], v[72:75]
	v_mfma_f32_16x16x32_bf16 v[68:71], v[208:211], v[192:195], v[68:71]
	s_setprio 0
	s_mov_b32 m0, s38
	v_lshl_add_u64 v[212:213], v[224:225], 0, s[60:61]
	s_barrier
	ds_read_b128 v[164:167], v150 offset:49152
	ds_read_b128 v[168:171], v150 offset:50176
	ds_read_b128 v[172:175], v150 offset:51200
	ds_read_b128 v[176:179], v150 offset:52224
	ds_read_b128 v[180:183], v150 offset:53248
	ds_read_b128 v[184:187], v150 offset:54272
	ds_read_b128 v[188:191], v150 offset:55296
	ds_read_b128 v[192:195], v150 offset:56320
	global_load_lds_dwordx4 v[212:213], off
	v_lshl_add_u64 v[212:213], v[230:231], 0, s[60:61]
	s_mov_b32 m0, s39
	s_nop 0
	global_load_lds_dwordx4 v[212:213], off
	s_barrier
	s_waitcnt lgkmcnt(0)
	s_setprio 1
	s_waitcnt lgkmcnt(0)
	v_mfma_f32_16x16x32_bf16 v[64:67], v[144:147], v[164:167], v[64:67]
	v_mfma_f32_16x16x32_bf16 v[60:63], v[156:159], v[164:167], v[60:63]
	v_mfma_f32_16x16x32_bf16 v[48:51], v[144:147], v[172:175], v[48:51]
	v_mfma_f32_16x16x32_bf16 v[44:47], v[156:159], v[172:175], v[44:47]
	v_mfma_f32_16x16x32_bf16 v[32:35], v[144:147], v[180:183], v[32:35]
	v_mfma_f32_16x16x32_bf16 v[28:31], v[156:159], v[180:183], v[28:31]
	v_mfma_f32_16x16x32_bf16 v[16:19], v[144:147], v[188:191], v[16:19]
	v_mfma_f32_16x16x32_bf16 v[12:15], v[156:159], v[188:191], v[12:15]
	v_mfma_f32_16x16x32_bf16 v[64:67], v[152:155], v[168:171], v[64:67]
	v_mfma_f32_16x16x32_bf16 v[60:63], v[160:163], v[168:171], v[60:63]
	v_mfma_f32_16x16x32_bf16 v[48:51], v[152:155], v[176:179], v[48:51]
	v_mfma_f32_16x16x32_bf16 v[44:47], v[160:163], v[176:179], v[44:47]
	v_mfma_f32_16x16x32_bf16 v[32:35], v[152:155], v[184:187], v[32:35]
	v_mfma_f32_16x16x32_bf16 v[28:31], v[160:163], v[184:187], v[28:31]
	v_mfma_f32_16x16x32_bf16 v[16:19], v[152:155], v[192:195], v[16:19]
	v_mfma_f32_16x16x32_bf16 v[12:15], v[160:163], v[192:195], v[12:15]
	s_setprio 0
	s_barrier
	s_add_u32 s16, s20, 0x40080
	s_addc_u32 s17, s21, 0
	s_add_i32 s20, s22, s29
	v_lshl_add_u64 v[144:145], s[16:17], 0, v[136:137]
	s_mov_b32 m0, s20
	s_nop 0
	global_load_lds_dwordx4 v[144:145], off
	v_lshl_add_u64 v[144:145], s[16:17], 0, v[132:133]
	s_add_i32 m0, s20, 0x2000
	s_nop 0
	global_load_lds_dwordx4 v[144:145], off
	s_waitcnt vmcnt(6)
	s_barrier
	s_setprio 1
	v_mfma_f32_16x16x32_bf16 v[56:59], v[196:199], v[164:167], v[56:59]
	v_mfma_f32_16x16x32_bf16 v[52:55], v[204:207], v[164:167], v[52:55]
	v_mfma_f32_16x16x32_bf16 v[40:43], v[196:199], v[172:175], v[40:43]
	v_mfma_f32_16x16x32_bf16 v[36:39], v[204:207], v[172:175], v[36:39]
	v_mfma_f32_16x16x32_bf16 v[24:27], v[196:199], v[180:183], v[24:27]
	v_mfma_f32_16x16x32_bf16 v[20:23], v[204:207], v[180:183], v[20:23]
	v_mfma_f32_16x16x32_bf16 v[8:11], v[196:199], v[188:191], v[8:11]
	v_mfma_f32_16x16x32_bf16 v[4:7], v[204:207], v[188:191], v[4:7]
	v_mfma_f32_16x16x32_bf16 v[56:59], v[200:203], v[168:171], v[56:59]
	v_mfma_f32_16x16x32_bf16 v[52:55], v[208:211], v[168:171], v[52:55]
	v_mfma_f32_16x16x32_bf16 v[40:43], v[200:203], v[176:179], v[40:43]
	v_mfma_f32_16x16x32_bf16 v[36:39], v[208:211], v[176:179], v[36:39]
	v_mfma_f32_16x16x32_bf16 v[24:27], v[200:203], v[184:187], v[24:27]
	v_mfma_f32_16x16x32_bf16 v[20:23], v[208:211], v[184:187], v[20:23]
	v_mfma_f32_16x16x32_bf16 v[8:11], v[200:203], v[192:195], v[8:11]
	v_mfma_f32_16x16x32_bf16 v[4:7], v[208:211], v[192:195], v[4:7]
	s_setprio 0
	s_add_i32 s45, s45, 2
	s_add_u32 s7, s7, 0x100
	s_addc_u32 s44, s44, 0
	s_cmp_gt_u32 s45, 13
	s_mov_b64 s[16:17], s[18:19]
	s_barrier
	s_cbranch_scc0 .LBB0_2136
	v_mov_b32_e32 v2, v148
	s_lshl_b32 s7, s43, 8
	s_add_i32 s7, s7, s37
	v_and_b32_e32 v145, 64, v214
	v_bfe_u32 v153, v2, 4, 2
	v_and_or_b32 v144, v2, 15, s7
	v_xor_b32_e32 v2, 16, v214
	v_add_u32_e32 v145, 64, v145
	v_cmp_lt_i32_e32 vcc, v2, v145
	s_lshl_b32 s18, s42, 8
	s_ashr_i32 s19, s18, 31
	v_cndmask_b32_e32 v2, v214, v2, vcc
	v_lshlrev_b32_e32 v152, 2, v2
	v_xor_b32_e32 v2, 32, v214
	v_cmp_lt_i32_e32 vcc, v2, v145
	v_ashrrev_i32_e32 v145, 31, v144
	v_lshlrev_b64 v[146:147], 11, v[144:145]
	v_lshl_add_u64 v[146:147], s[4:5], 0, v[146:147]
	v_cndmask_b32_e32 v2, v214, v2, vcc
	v_lshl_add_u64 v[146:147], s[18:19], 1, v[146:147]
	v_lshlrev_b32_e32 v151, 2, v2
	v_lshl_add_u64 v[146:147], v[146:147], 0, s[50:51]
	v_lshlrev_b32_e32 v2, 4, v153
	v_lshl_add_u64 v[146:147], v[146:147], 0, v[2:3]
	global_load_dwordx4 v[160:163], v[146:147], off
	global_load_dwordx4 v[164:167], v[146:147], off offset:256
	s_mov_b32 s100, 0x8000
	s_mov_b32 s101, 0
	v_lshl_add_u64 v[210:211], v[146:147], 0, s[100:101]
	global_load_dwordx4 v[168:171], v[210:211], off
	global_load_dwordx4 v[172:175], v[210:211], off offset:256
	v_lshl_add_u64 v[210:211], v[210:211], 0, s[100:101]
	global_load_dwordx4 v[176:179], v[210:211], off
	global_load_dwordx4 v[180:183], v[210:211], off offset:256
	v_lshl_add_u64 v[210:211], v[210:211], 0, s[100:101]
	global_load_dwordx4 v[184:187], v[210:211], off
	global_load_dwordx4 v[188:191], v[210:211], off offset:256
	s_mov_b32 s100, 0x28000
	v_lshl_add_u64 v[210:211], v[210:211], 0, s[100:101]
	global_load_dwordx4 v[192:195], v[210:211], off
	global_load_dwordx4 v[198:201], v[210:211], off offset:256
	s_mov_b32 s100, 0x8000
	v_lshl_add_u64 v[210:211], v[210:211], 0, s[100:101]
	global_load_dwordx4 v[202:205], v[210:211], off
	global_load_dwordx4 v[206:209], v[210:211], off offset:256
	v_lshl_add_u64 v[210:211], v[210:211], 0, s[100:101]
	global_load_dwordx4 v[236:239], v[210:211], off
	global_load_dwordx4 v[240:243], v[210:211], off offset:256
	v_lshl_add_u64 v[210:211], v[210:211], 0, s[100:101]
	global_load_dwordx4 v[244:247], v[210:211], off
	global_load_dwordx4 v[248:251], v[210:211], off offset:256
	s_waitcnt vmcnt(0)
	v_mov_b32_e32 v154, v160
	v_mov_b32_e32 v155, v161
	v_mov_b32_e32 v156, v162
	v_mov_b32_e32 v157, v163
	s_lshl_b32 s16, s42, 2
	v_cmp_eq_u32_e32 vcc, 0, v153
	s_ashr_i32 s17, s16, 31
	v_lshlrev_b32_e32 v158, 16, v154
	v_and_b32_e32 v159, 0xffff0000, v154
	v_lshlrev_b32_e32 v154, 16, v155
	v_and_b32_e32 v155, 0xffff0000, v155
	v_pk_add_f32 v[130:131], v[130:131], v[154:155]
	v_lshlrev_b32_e32 v154, 16, v156
	v_and_b32_e32 v155, 0xffff0000, v156
	v_lshlrev_b32_e32 v156, 16, v157
	v_and_b32_e32 v157, 0xffff0000, v157
	v_pk_add_f32 v[128:129], v[128:129], v[158:159]
	v_pk_add_f32 v[156:157], v[126:127], v[156:157]
	v_pk_add_f32 v[154:155], v[124:125], v[154:155]
	v_cvt_pk_bf16_f32 v124, v128, v129
	v_cvt_pk_bf16_f32 v125, v130, v131
	v_cvt_pk_bf16_f32 v126, v154, v155
	v_cvt_pk_bf16_f32 v127, v156, v157
	global_store_dwordx4 v[146:147], v[124:127], off
	v_mul_f32_e32 v2, v129, v129
	v_fmac_f32_e32 v2, v128, v128
	v_mul_f32_e32 v124, v131, v131
	v_fmac_f32_e32 v124, v130, v130
	v_add_f32_e32 v2, v2, v124
	v_mul_f32_e32 v124, v155, v155
	v_fmac_f32_e32 v124, v154, v154
	v_add_f32_e32 v2, v124, v2
	v_mul_f32_e32 v124, v157, v157
	v_fmac_f32_e32 v124, v156, v156
	v_add_f32_e32 v2, v124, v2
	v_mov_b32_e32 v124, v164
	v_mov_b32_e32 v125, v165
	v_mov_b32_e32 v126, v166
	v_mov_b32_e32 v127, v167
	v_lshlrev_b32_e32 v128, 16, v124
	v_and_b32_e32 v129, 0xffff0000, v124
	v_lshlrev_b32_e32 v124, 16, v125
	v_and_b32_e32 v125, 0xffff0000, v125
	v_pk_add_f32 v[122:123], v[122:123], v[124:125]
	v_lshlrev_b32_e32 v124, 16, v126
	v_and_b32_e32 v125, 0xffff0000, v126
	v_lshlrev_b32_e32 v126, 16, v127
	v_and_b32_e32 v127, 0xffff0000, v127
	v_pk_add_f32 v[120:121], v[120:121], v[128:129]
	v_pk_add_f32 v[126:127], v[118:119], v[126:127]
	v_pk_add_f32 v[124:125], v[116:117], v[124:125]
	v_cvt_pk_bf16_f32 v116, v120, v121
	v_cvt_pk_bf16_f32 v117, v122, v123
	v_cvt_pk_bf16_f32 v118, v124, v125
	v_cvt_pk_bf16_f32 v119, v126, v127
	global_store_dwordx4 v[146:147], v[116:119], off offset:256
	s_nop 1
	v_mul_f32_e32 v116, v121, v121
	v_mul_f32_e32 v117, v123, v123
	v_fmac_f32_e32 v116, v120, v120
	v_fmac_f32_e32 v117, v122, v122
	v_add_f32_e32 v116, v116, v117
	v_mul_f32_e32 v117, v125, v125
	v_fmac_f32_e32 v117, v124, v124
	v_add_f32_e32 v116, v117, v116
	v_mul_f32_e32 v117, v127, v127
	v_fmac_f32_e32 v117, v126, v126
	v_add_f32_e32 v116, v117, v116
	v_add_f32_e32 v2, v2, v116
	ds_bpermute_b32 v116, v152, v2
	s_waitcnt lgkmcnt(0)
	v_add_f32_e32 v2, v2, v116
	ds_bpermute_b32 v116, v151, v2
	s_and_saveexec_b64 s[20:21], vcc
	s_cbranch_execz .LBB0_2139
	v_lshlrev_b64 v[118:119], 6, v[144:145]
	v_lshl_add_u64 v[118:119], s[2:3], 0, v[118:119]
	v_lshl_add_u64 v[118:119], s[16:17], 2, v[118:119]
	s_lshl_b32 s22, s36, 2
	s_mov_b32 s23, s51
	v_lshl_add_u64 v[118:119], v[118:119], 0, s[22:23]
	s_waitcnt lgkmcnt(0)
	v_add_f32_e32 v2, v2, v116
	global_store_dword v[118:119], v2, off
.LBB0_2139:
	s_or_b64 exec, exec, s[20:21]
	s_waitcnt lgkmcnt(0)
	v_or_b32_e32 v116, 16, v144
	v_ashrrev_i32_e32 v117, 31, v116
	v_lshlrev_b64 v[118:119], 11, v[116:117]
	v_lshl_add_u64 v[118:119], s[4:5], 0, v[118:119]
	v_lshlrev_b32_e32 v2, 3, v153
	v_lshl_add_u64 v[118:119], s[18:19], 1, v[118:119]
	v_lshl_add_u64 v[118:119], v[118:119], 0, s[50:51]
	v_lshlrev_b32_e32 v2, 1, v2
	v_lshl_add_u64 v[118:119], v[118:119], 0, v[2:3]
	v_mov_b32_e32 v120, v168
	v_mov_b32_e32 v121, v169
	v_mov_b32_e32 v122, v170
	v_mov_b32_e32 v123, v171
	v_lshlrev_b32_e32 v124, 16, v120
	v_and_b32_e32 v125, 0xffff0000, v120
	v_lshlrev_b32_e32 v120, 16, v121
	v_and_b32_e32 v121, 0xffff0000, v121
	v_pk_add_f32 v[114:115], v[114:115], v[120:121]
	v_lshlrev_b32_e32 v120, 16, v122
	v_and_b32_e32 v121, 0xffff0000, v122
	v_lshlrev_b32_e32 v122, 16, v123
	v_and_b32_e32 v123, 0xffff0000, v123
	v_pk_add_f32 v[112:113], v[112:113], v[124:125]
	v_pk_add_f32 v[122:123], v[110:111], v[122:123]
	v_pk_add_f32 v[120:121], v[108:109], v[120:121]
	v_cvt_pk_bf16_f32 v108, v112, v113
	v_cvt_pk_bf16_f32 v109, v114, v115
	v_cvt_pk_bf16_f32 v110, v120, v121
	v_cvt_pk_bf16_f32 v111, v122, v123
	global_store_dwordx4 v[118:119], v[108:111], off
	s_nop 1
	v_mul_f32_e32 v108, v113, v113
	v_mul_f32_e32 v109, v115, v115
	v_fmac_f32_e32 v108, v112, v112
	v_fmac_f32_e32 v109, v114, v114
	v_add_f32_e32 v108, v108, v109
	v_mul_f32_e32 v109, v121, v121
	v_fmac_f32_e32 v109, v120, v120
	v_add_f32_e32 v108, v109, v108
	v_mul_f32_e32 v109, v123, v123
	v_fmac_f32_e32 v109, v122, v122
	v_add_f32_e32 v114, v109, v108
	v_mov_b32_e32 v108, v172
	v_mov_b32_e32 v109, v173
	v_mov_b32_e32 v110, v174
	v_mov_b32_e32 v111, v175
	v_lshlrev_b32_e32 v112, 16, v108
	v_and_b32_e32 v113, 0xffff0000, v108
	v_lshlrev_b32_e32 v108, 16, v109
	v_and_b32_e32 v109, 0xffff0000, v109
	v_pk_add_f32 v[106:107], v[106:107], v[108:109]
	v_lshlrev_b32_e32 v108, 16, v110
	v_and_b32_e32 v109, 0xffff0000, v110
	v_lshlrev_b32_e32 v110, 16, v111
	v_and_b32_e32 v111, 0xffff0000, v111
	v_pk_add_f32 v[104:105], v[104:105], v[112:113]
	v_pk_add_f32 v[110:111], v[102:103], v[110:111]
	v_pk_add_f32 v[108:109], v[100:101], v[108:109]
	v_cvt_pk_bf16_f32 v100, v104, v105
	v_cvt_pk_bf16_f32 v101, v106, v107
	v_cvt_pk_bf16_f32 v102, v108, v109
	v_cvt_pk_bf16_f32 v103, v110, v111
	global_store_dwordx4 v[118:119], v[100:103], off offset:256
	s_nop 1
	v_mul_f32_e32 v100, v105, v105
	v_mul_f32_e32 v101, v107, v107
	v_fmac_f32_e32 v100, v104, v104
	v_fmac_f32_e32 v101, v106, v106
	v_add_f32_e32 v100, v100, v101
	v_mul_f32_e32 v101, v109, v109
	v_fmac_f32_e32 v101, v108, v108
	v_add_f32_e32 v100, v101, v100
	v_mul_f32_e32 v101, v111, v111
	v_fmac_f32_e32 v101, v110, v110
	v_add_f32_e32 v100, v101, v100
	v_add_f32_e32 v100, v114, v100
	ds_bpermute_b32 v101, v152, v100
	s_waitcnt lgkmcnt(0)
	v_add_f32_e32 v100, v100, v101
	ds_bpermute_b32 v101, v151, v100
	s_and_saveexec_b64 s[20:21], vcc
	s_cbranch_execz .LBB0_2141
	v_lshlrev_b64 v[102:103], 6, v[116:117]
	v_lshl_add_u64 v[102:103], s[2:3], 0, v[102:103]
	v_lshl_add_u64 v[102:103], s[16:17], 2, v[102:103]
	s_lshl_b32 s22, s36, 2
	s_mov_b32 s23, s51
	v_lshl_add_u64 v[102:103], v[102:103], 0, s[22:23]
	s_waitcnt lgkmcnt(0)
	v_add_f32_e32 v100, v100, v101
	global_store_dword v[102:103], v100, off
.LBB0_2141:
	s_or_b64 exec, exec, s[20:21]
	v_or_b32_e32 v100, 32, v144
	s_waitcnt lgkmcnt(0)
	v_ashrrev_i32_e32 v101, 31, v100
	v_lshlrev_b64 v[102:103], 11, v[100:101]
	v_lshl_add_u64 v[102:103], s[4:5], 0, v[102:103]
	v_lshl_add_u64 v[102:103], s[18:19], 1, v[102:103]
	v_lshl_add_u64 v[102:103], v[102:103], 0, s[50:51]
	v_lshl_add_u64 v[102:103], v[102:103], 0, v[2:3]
	v_mov_b32_e32 v104, v176
	v_mov_b32_e32 v105, v177
	v_mov_b32_e32 v106, v178
	v_mov_b32_e32 v107, v179
	v_lshlrev_b32_e32 v108, 16, v104
	v_and_b32_e32 v109, 0xffff0000, v104
	v_lshlrev_b32_e32 v104, 16, v105
	v_and_b32_e32 v105, 0xffff0000, v105
	v_pk_add_f32 v[98:99], v[98:99], v[104:105]
	v_lshlrev_b32_e32 v104, 16, v106
	v_and_b32_e32 v105, 0xffff0000, v106
	v_lshlrev_b32_e32 v106, 16, v107
	v_and_b32_e32 v107, 0xffff0000, v107
	v_pk_add_f32 v[96:97], v[96:97], v[108:109]
	v_pk_add_f32 v[106:107], v[94:95], v[106:107]
	v_pk_add_f32 v[104:105], v[92:93], v[104:105]
	v_cvt_pk_bf16_f32 v92, v96, v97
	v_cvt_pk_bf16_f32 v93, v98, v99
	v_cvt_pk_bf16_f32 v94, v104, v105
	v_cvt_pk_bf16_f32 v95, v106, v107
	global_store_dwordx4 v[102:103], v[92:95], off
	s_nop 1
	v_mul_f32_e32 v92, v97, v97
	v_mul_f32_e32 v93, v99, v99
	v_fmac_f32_e32 v92, v96, v96
	v_fmac_f32_e32 v93, v98, v98
	v_add_f32_e32 v92, v92, v93
	v_mul_f32_e32 v93, v105, v105
	v_fmac_f32_e32 v93, v104, v104
	v_add_f32_e32 v92, v93, v92
	v_mul_f32_e32 v93, v107, v107
	v_fmac_f32_e32 v93, v106, v106
	v_add_f32_e32 v98, v93, v92
	v_mov_b32_e32 v92, v180
	v_mov_b32_e32 v93, v181
	v_mov_b32_e32 v94, v182
	v_mov_b32_e32 v95, v183
	v_lshlrev_b32_e32 v96, 16, v92
	v_and_b32_e32 v97, 0xffff0000, v92
	v_lshlrev_b32_e32 v92, 16, v93
	v_and_b32_e32 v93, 0xffff0000, v93
	v_pk_add_f32 v[90:91], v[90:91], v[92:93]
	v_lshlrev_b32_e32 v92, 16, v94
	v_and_b32_e32 v93, 0xffff0000, v94
	v_lshlrev_b32_e32 v94, 16, v95
	v_and_b32_e32 v95, 0xffff0000, v95
	v_pk_add_f32 v[88:89], v[88:89], v[96:97]
	v_pk_add_f32 v[94:95], v[86:87], v[94:95]
	v_pk_add_f32 v[92:93], v[84:85], v[92:93]
	v_cvt_pk_bf16_f32 v84, v88, v89
	v_cvt_pk_bf16_f32 v85, v90, v91
	v_cvt_pk_bf16_f32 v86, v92, v93
	v_cvt_pk_bf16_f32 v87, v94, v95
	global_store_dwordx4 v[102:103], v[84:87], off offset:256
	s_nop 1
	v_mul_f32_e32 v84, v89, v89
	v_mul_f32_e32 v85, v91, v91
	v_fmac_f32_e32 v84, v88, v88
	v_fmac_f32_e32 v85, v90, v90
	v_add_f32_e32 v84, v84, v85
	v_mul_f32_e32 v85, v93, v93
	v_fmac_f32_e32 v85, v92, v92
	v_add_f32_e32 v84, v85, v84
	v_mul_f32_e32 v85, v95, v95
	v_fmac_f32_e32 v85, v94, v94
	v_add_f32_e32 v84, v85, v84
	v_add_f32_e32 v84, v98, v84
	ds_bpermute_b32 v85, v152, v84
	s_waitcnt lgkmcnt(0)
	v_add_f32_e32 v84, v84, v85
	ds_bpermute_b32 v85, v151, v84
	s_and_saveexec_b64 s[20:21], vcc
	s_cbranch_execz .LBB0_2143
	v_lshlrev_b64 v[86:87], 6, v[100:101]
	v_lshl_add_u64 v[86:87], s[2:3], 0, v[86:87]
	v_lshl_add_u64 v[86:87], s[16:17], 2, v[86:87]
	s_lshl_b32 s22, s36, 2
	s_mov_b32 s23, s51
	v_lshl_add_u64 v[86:87], v[86:87], 0, s[22:23]
	s_waitcnt lgkmcnt(0)
	v_add_f32_e32 v84, v84, v85
	global_store_dword v[86:87], v84, off
.LBB0_2143:
	s_or_b64 exec, exec, s[20:21]
	v_or_b32_e32 v84, 48, v144
	s_waitcnt lgkmcnt(0)
	v_ashrrev_i32_e32 v85, 31, v84
	v_lshlrev_b64 v[86:87], 11, v[84:85]
	v_lshl_add_u64 v[86:87], s[4:5], 0, v[86:87]
	v_lshl_add_u64 v[86:87], s[18:19], 1, v[86:87]
	v_lshl_add_u64 v[86:87], v[86:87], 0, s[50:51]
	v_lshl_add_u64 v[86:87], v[86:87], 0, v[2:3]
	v_mov_b32_e32 v88, v184
	v_mov_b32_e32 v89, v185
	v_mov_b32_e32 v90, v186
	v_mov_b32_e32 v91, v187
	v_lshlrev_b32_e32 v92, 16, v88
	v_and_b32_e32 v93, 0xffff0000, v88
	v_lshlrev_b32_e32 v88, 16, v89
	v_and_b32_e32 v89, 0xffff0000, v89
	v_pk_add_f32 v[82:83], v[82:83], v[88:89]
	v_lshlrev_b32_e32 v88, 16, v90
	v_and_b32_e32 v89, 0xffff0000, v90
	v_lshlrev_b32_e32 v90, 16, v91
	v_and_b32_e32 v91, 0xffff0000, v91
	v_pk_add_f32 v[80:81], v[80:81], v[92:93]
	v_pk_add_f32 v[90:91], v[78:79], v[90:91]
	v_pk_add_f32 v[88:89], v[76:77], v[88:89]
	v_cvt_pk_bf16_f32 v76, v80, v81
	v_cvt_pk_bf16_f32 v77, v82, v83
	v_cvt_pk_bf16_f32 v78, v88, v89
	v_cvt_pk_bf16_f32 v79, v90, v91
	global_store_dwordx4 v[86:87], v[76:79], off
	s_nop 1
	v_mul_f32_e32 v76, v81, v81
	v_mul_f32_e32 v77, v83, v83
	v_fmac_f32_e32 v76, v80, v80
	v_fmac_f32_e32 v77, v82, v82
	v_add_f32_e32 v76, v76, v77
	v_mul_f32_e32 v77, v89, v89
	v_fmac_f32_e32 v77, v88, v88
	v_add_f32_e32 v76, v77, v76
	v_mul_f32_e32 v77, v91, v91
	v_fmac_f32_e32 v77, v90, v90
	v_add_f32_e32 v82, v77, v76
	v_mov_b32_e32 v76, v188
	v_mov_b32_e32 v77, v189
	v_mov_b32_e32 v78, v190
	v_mov_b32_e32 v79, v191
	v_lshlrev_b32_e32 v80, 16, v76
	v_and_b32_e32 v81, 0xffff0000, v76
	v_lshlrev_b32_e32 v76, 16, v77
	v_and_b32_e32 v77, 0xffff0000, v77
	v_pk_add_f32 v[74:75], v[74:75], v[76:77]
	v_lshlrev_b32_e32 v76, 16, v78
	v_and_b32_e32 v77, 0xffff0000, v78
	v_lshlrev_b32_e32 v78, 16, v79
	v_and_b32_e32 v79, 0xffff0000, v79
	v_pk_add_f32 v[72:73], v[72:73], v[80:81]
	v_pk_add_f32 v[78:79], v[70:71], v[78:79]
	v_pk_add_f32 v[76:77], v[68:69], v[76:77]
	v_cvt_pk_bf16_f32 v68, v72, v73
	v_cvt_pk_bf16_f32 v69, v74, v75
	v_cvt_pk_bf16_f32 v70, v76, v77
	v_cvt_pk_bf16_f32 v71, v78, v79
	global_store_dwordx4 v[86:87], v[68:71], off offset:256
	s_nop 1
	v_mul_f32_e32 v68, v73, v73
	v_mul_f32_e32 v69, v75, v75
	v_fmac_f32_e32 v68, v72, v72
	v_fmac_f32_e32 v69, v74, v74
	v_add_f32_e32 v68, v68, v69
	v_mul_f32_e32 v69, v77, v77
	v_fmac_f32_e32 v69, v76, v76
	v_add_f32_e32 v68, v69, v68
	v_mul_f32_e32 v69, v79, v79
	v_fmac_f32_e32 v69, v78, v78
	v_add_f32_e32 v68, v69, v68
	v_add_f32_e32 v68, v82, v68
	ds_bpermute_b32 v69, v152, v68
	s_waitcnt lgkmcnt(0)
	v_add_f32_e32 v68, v68, v69
	ds_bpermute_b32 v69, v151, v68
	s_and_saveexec_b64 s[20:21], vcc
	s_cbranch_execz .LBB0_2145
	v_lshlrev_b64 v[70:71], 6, v[84:85]
	v_lshl_add_u64 v[70:71], s[2:3], 0, v[70:71]
	v_lshl_add_u64 v[70:71], s[16:17], 2, v[70:71]
	s_lshl_b32 s22, s36, 2
	s_mov_b32 s23, s51
	v_lshl_add_u64 v[70:71], v[70:71], 0, s[22:23]
	s_waitcnt lgkmcnt(0)
	v_add_f32_e32 v68, v68, v69
	global_store_dword v[70:71], v68, off
.LBB0_2145:
	s_or_b64 exec, exec, s[20:21]
	v_add_u32_e32 v68, 0x80, v144
	s_waitcnt lgkmcnt(0)
	v_ashrrev_i32_e32 v69, 31, v68
	v_lshlrev_b64 v[70:71], 11, v[68:69]
	v_lshl_add_u64 v[70:71], s[4:5], 0, v[70:71]
	v_lshl_add_u64 v[70:71], s[18:19], 1, v[70:71]
	v_lshl_add_u64 v[70:71], v[70:71], 0, s[50:51]
	v_lshl_add_u64 v[70:71], v[70:71], 0, v[2:3]
	v_mov_b32_e32 v72, v192
	v_mov_b32_e32 v73, v193
	v_mov_b32_e32 v74, v194
	v_mov_b32_e32 v75, v195
	v_lshlrev_b32_e32 v76, 16, v72
	v_and_b32_e32 v77, 0xffff0000, v72
	v_lshlrev_b32_e32 v72, 16, v73
	v_and_b32_e32 v73, 0xffff0000, v73
	v_pk_add_f32 v[66:67], v[66:67], v[72:73]
	v_lshlrev_b32_e32 v72, 16, v74
	v_and_b32_e32 v73, 0xffff0000, v74
	v_lshlrev_b32_e32 v74, 16, v75
	v_and_b32_e32 v75, 0xffff0000, v75
	v_pk_add_f32 v[64:65], v[64:65], v[76:77]
	v_pk_add_f32 v[74:75], v[62:63], v[74:75]
	v_pk_add_f32 v[72:73], v[60:61], v[72:73]
	v_cvt_pk_bf16_f32 v60, v64, v65
	v_cvt_pk_bf16_f32 v61, v66, v67
	v_cvt_pk_bf16_f32 v62, v72, v73
	v_cvt_pk_bf16_f32 v63, v74, v75
	global_store_dwordx4 v[70:71], v[60:63], off
	s_nop 1
	v_mul_f32_e32 v60, v65, v65
	v_mul_f32_e32 v61, v67, v67
	v_fmac_f32_e32 v60, v64, v64
	v_fmac_f32_e32 v61, v66, v66
	v_add_f32_e32 v60, v60, v61
	v_mul_f32_e32 v61, v73, v73
	v_fmac_f32_e32 v61, v72, v72
	v_add_f32_e32 v60, v61, v60
	v_mul_f32_e32 v61, v75, v75
	v_fmac_f32_e32 v61, v74, v74
	v_add_f32_e32 v66, v61, v60
	v_mov_b32_e32 v60, v198
	v_mov_b32_e32 v61, v199
	v_mov_b32_e32 v62, v200
	v_mov_b32_e32 v63, v201
	v_lshlrev_b32_e32 v64, 16, v60
	v_and_b32_e32 v65, 0xffff0000, v60
	v_lshlrev_b32_e32 v60, 16, v61
	v_and_b32_e32 v61, 0xffff0000, v61
	v_pk_add_f32 v[58:59], v[58:59], v[60:61]
	v_lshlrev_b32_e32 v60, 16, v62
	v_and_b32_e32 v61, 0xffff0000, v62
	v_lshlrev_b32_e32 v62, 16, v63
	v_and_b32_e32 v63, 0xffff0000, v63
	v_pk_add_f32 v[56:57], v[56:57], v[64:65]
	v_pk_add_f32 v[62:63], v[54:55], v[62:63]
	v_pk_add_f32 v[60:61], v[52:53], v[60:61]
	v_cvt_pk_bf16_f32 v52, v56, v57
	v_cvt_pk_bf16_f32 v53, v58, v59
	v_cvt_pk_bf16_f32 v54, v60, v61
	v_cvt_pk_bf16_f32 v55, v62, v63
	global_store_dwordx4 v[70:71], v[52:55], off offset:256
	s_nop 1
	v_mul_f32_e32 v52, v57, v57
	v_mul_f32_e32 v53, v59, v59
	v_fmac_f32_e32 v52, v56, v56
	v_fmac_f32_e32 v53, v58, v58
	v_add_f32_e32 v52, v52, v53
	v_mul_f32_e32 v53, v61, v61
	v_fmac_f32_e32 v53, v60, v60
	v_add_f32_e32 v52, v53, v52
	v_mul_f32_e32 v53, v63, v63
	v_fmac_f32_e32 v53, v62, v62
	v_add_f32_e32 v52, v53, v52
	v_add_f32_e32 v52, v66, v52
	ds_bpermute_b32 v53, v152, v52
	s_waitcnt lgkmcnt(0)
	v_add_f32_e32 v52, v52, v53
	ds_bpermute_b32 v53, v151, v52
	s_and_saveexec_b64 s[20:21], vcc
	s_cbranch_execz .LBB0_2147
	v_lshlrev_b64 v[54:55], 6, v[68:69]
	v_lshl_add_u64 v[54:55], s[2:3], 0, v[54:55]
	v_lshl_add_u64 v[54:55], s[16:17], 2, v[54:55]
	s_lshl_b32 s22, s36, 2
	s_mov_b32 s23, s51
	v_lshl_add_u64 v[54:55], v[54:55], 0, s[22:23]
	s_waitcnt lgkmcnt(0)
	v_add_f32_e32 v52, v52, v53
	global_store_dword v[54:55], v52, off
.LBB0_2147:
	s_or_b64 exec, exec, s[20:21]
	v_add_u32_e32 v52, 0x90, v144
	s_waitcnt lgkmcnt(0)
	v_ashrrev_i32_e32 v53, 31, v52
	v_lshlrev_b64 v[54:55], 11, v[52:53]
	v_lshl_add_u64 v[54:55], s[4:5], 0, v[54:55]
	v_lshl_add_u64 v[54:55], s[18:19], 1, v[54:55]
	v_lshl_add_u64 v[54:55], v[54:55], 0, s[50:51]
	v_lshl_add_u64 v[54:55], v[54:55], 0, v[2:3]
	v_mov_b32_e32 v56, v202
	v_mov_b32_e32 v57, v203
	v_mov_b32_e32 v58, v204
	v_mov_b32_e32 v59, v205
	v_lshlrev_b32_e32 v60, 16, v56
	v_and_b32_e32 v61, 0xffff0000, v56
	v_lshlrev_b32_e32 v56, 16, v57
	v_and_b32_e32 v57, 0xffff0000, v57
	v_pk_add_f32 v[50:51], v[50:51], v[56:57]
	v_lshlrev_b32_e32 v56, 16, v58
	v_and_b32_e32 v57, 0xffff0000, v58
	v_lshlrev_b32_e32 v58, 16, v59
	v_and_b32_e32 v59, 0xffff0000, v59
	v_pk_add_f32 v[48:49], v[48:49], v[60:61]
	v_pk_add_f32 v[58:59], v[46:47], v[58:59]
	v_pk_add_f32 v[56:57], v[44:45], v[56:57]
	v_cvt_pk_bf16_f32 v44, v48, v49
	v_cvt_pk_bf16_f32 v45, v50, v51
	v_cvt_pk_bf16_f32 v46, v56, v57
	v_cvt_pk_bf16_f32 v47, v58, v59
	global_store_dwordx4 v[54:55], v[44:47], off
	s_nop 1
	v_mul_f32_e32 v44, v49, v49
	v_mul_f32_e32 v45, v51, v51
	v_fmac_f32_e32 v44, v48, v48
	v_fmac_f32_e32 v45, v50, v50
	v_add_f32_e32 v44, v44, v45
	v_mul_f32_e32 v45, v57, v57
	v_fmac_f32_e32 v45, v56, v56
	v_add_f32_e32 v44, v45, v44
	v_mul_f32_e32 v45, v59, v59
	v_fmac_f32_e32 v45, v58, v58
	v_add_f32_e32 v50, v45, v44
	v_mov_b32_e32 v44, v206
	v_mov_b32_e32 v45, v207
	v_mov_b32_e32 v46, v208
	v_mov_b32_e32 v47, v209
	v_lshlrev_b32_e32 v48, 16, v44
	v_and_b32_e32 v49, 0xffff0000, v44
	v_lshlrev_b32_e32 v44, 16, v45
	v_and_b32_e32 v45, 0xffff0000, v45
	v_pk_add_f32 v[42:43], v[42:43], v[44:45]
	v_lshlrev_b32_e32 v44, 16, v46
	v_and_b32_e32 v45, 0xffff0000, v46
	v_lshlrev_b32_e32 v46, 16, v47
	v_and_b32_e32 v47, 0xffff0000, v47
	v_pk_add_f32 v[40:41], v[40:41], v[48:49]
	v_pk_add_f32 v[46:47], v[38:39], v[46:47]
	v_pk_add_f32 v[44:45], v[36:37], v[44:45]
	v_cvt_pk_bf16_f32 v36, v40, v41
	v_cvt_pk_bf16_f32 v37, v42, v43
	v_cvt_pk_bf16_f32 v38, v44, v45
	v_cvt_pk_bf16_f32 v39, v46, v47
	global_store_dwordx4 v[54:55], v[36:39], off offset:256
	s_nop 1
	v_mul_f32_e32 v36, v41, v41
	v_mul_f32_e32 v37, v43, v43
	v_fmac_f32_e32 v36, v40, v40
	v_fmac_f32_e32 v37, v42, v42
	v_add_f32_e32 v36, v36, v37
	v_mul_f32_e32 v37, v45, v45
	v_fmac_f32_e32 v37, v44, v44
	v_add_f32_e32 v36, v37, v36
	v_mul_f32_e32 v37, v47, v47
	v_fmac_f32_e32 v37, v46, v46
	v_add_f32_e32 v36, v37, v36
	v_add_f32_e32 v36, v50, v36
	ds_bpermute_b32 v37, v152, v36
	s_waitcnt lgkmcnt(0)
	v_add_f32_e32 v36, v36, v37
	ds_bpermute_b32 v37, v151, v36
	s_and_saveexec_b64 s[20:21], vcc
	s_cbranch_execz .LBB0_2149
	v_lshlrev_b64 v[38:39], 6, v[52:53]
	v_lshl_add_u64 v[38:39], s[2:3], 0, v[38:39]
	v_lshl_add_u64 v[38:39], s[16:17], 2, v[38:39]
	s_lshl_b32 s22, s36, 2
	s_mov_b32 s23, s51
	v_lshl_add_u64 v[38:39], v[38:39], 0, s[22:23]
	s_waitcnt lgkmcnt(0)
	v_add_f32_e32 v36, v36, v37
	global_store_dword v[38:39], v36, off
.LBB0_2149:
	s_or_b64 exec, exec, s[20:21]
	v_add_u32_e32 v36, 0xa0, v144
	s_waitcnt lgkmcnt(0)
	v_ashrrev_i32_e32 v37, 31, v36
	v_lshlrev_b64 v[38:39], 11, v[36:37]
	v_lshl_add_u64 v[38:39], s[4:5], 0, v[38:39]
	v_lshl_add_u64 v[38:39], s[18:19], 1, v[38:39]
	v_lshl_add_u64 v[38:39], v[38:39], 0, s[50:51]
	v_lshl_add_u64 v[38:39], v[38:39], 0, v[2:3]
	v_mov_b32_e32 v40, v236
	v_mov_b32_e32 v41, v237
	v_mov_b32_e32 v42, v238
	v_mov_b32_e32 v43, v239
	v_lshlrev_b32_e32 v44, 16, v40
	v_and_b32_e32 v45, 0xffff0000, v40
	v_lshlrev_b32_e32 v40, 16, v41
	v_and_b32_e32 v41, 0xffff0000, v41
	v_pk_add_f32 v[34:35], v[34:35], v[40:41]
	v_lshlrev_b32_e32 v40, 16, v42
	v_and_b32_e32 v41, 0xffff0000, v42
	v_lshlrev_b32_e32 v42, 16, v43
	v_and_b32_e32 v43, 0xffff0000, v43
	v_pk_add_f32 v[32:33], v[32:33], v[44:45]
	v_pk_add_f32 v[42:43], v[30:31], v[42:43]
	v_pk_add_f32 v[40:41], v[28:29], v[40:41]
	v_cvt_pk_bf16_f32 v28, v32, v33
	v_cvt_pk_bf16_f32 v29, v34, v35
	v_cvt_pk_bf16_f32 v30, v40, v41
	v_cvt_pk_bf16_f32 v31, v42, v43
	global_store_dwordx4 v[38:39], v[28:31], off
	s_nop 1
	v_mul_f32_e32 v28, v33, v33
	v_mul_f32_e32 v29, v35, v35
	v_fmac_f32_e32 v28, v32, v32
	v_fmac_f32_e32 v29, v34, v34
	v_add_f32_e32 v28, v28, v29
	v_mul_f32_e32 v29, v41, v41
	v_fmac_f32_e32 v29, v40, v40
	v_add_f32_e32 v28, v29, v28
	v_mul_f32_e32 v29, v43, v43
	v_fmac_f32_e32 v29, v42, v42
	v_add_f32_e32 v34, v29, v28
	v_mov_b32_e32 v28, v240
	v_mov_b32_e32 v29, v241
	v_mov_b32_e32 v30, v242
	v_mov_b32_e32 v31, v243
	v_lshlrev_b32_e32 v32, 16, v28
	v_and_b32_e32 v33, 0xffff0000, v28
	v_lshlrev_b32_e32 v28, 16, v29
	v_and_b32_e32 v29, 0xffff0000, v29
	v_pk_add_f32 v[26:27], v[26:27], v[28:29]
	v_lshlrev_b32_e32 v28, 16, v30
	v_and_b32_e32 v29, 0xffff0000, v30
	v_lshlrev_b32_e32 v30, 16, v31
	v_and_b32_e32 v31, 0xffff0000, v31
	v_pk_add_f32 v[24:25], v[24:25], v[32:33]
	v_pk_add_f32 v[30:31], v[22:23], v[30:31]
	v_pk_add_f32 v[28:29], v[20:21], v[28:29]
	v_cvt_pk_bf16_f32 v20, v24, v25
	v_cvt_pk_bf16_f32 v21, v26, v27
	v_cvt_pk_bf16_f32 v22, v28, v29
	v_cvt_pk_bf16_f32 v23, v30, v31
	global_store_dwordx4 v[38:39], v[20:23], off offset:256
	s_nop 1
	v_mul_f32_e32 v20, v25, v25
	v_mul_f32_e32 v21, v27, v27
	v_fmac_f32_e32 v20, v24, v24
	v_fmac_f32_e32 v21, v26, v26
	v_add_f32_e32 v20, v20, v21
	v_mul_f32_e32 v21, v29, v29
	v_fmac_f32_e32 v21, v28, v28
	v_add_f32_e32 v20, v21, v20
	v_mul_f32_e32 v21, v31, v31
	v_fmac_f32_e32 v21, v30, v30
	v_add_f32_e32 v20, v21, v20
	v_add_f32_e32 v20, v34, v20
	ds_bpermute_b32 v21, v152, v20
	s_waitcnt lgkmcnt(0)
	v_add_f32_e32 v20, v20, v21
	ds_bpermute_b32 v21, v151, v20
	s_and_saveexec_b64 s[20:21], vcc
	s_cbranch_execz .LBB0_2151
	v_lshlrev_b64 v[22:23], 6, v[36:37]
	v_lshl_add_u64 v[22:23], s[2:3], 0, v[22:23]
	v_lshl_add_u64 v[22:23], s[16:17], 2, v[22:23]
	s_lshl_b32 s22, s36, 2
	s_mov_b32 s23, s51
	v_lshl_add_u64 v[22:23], v[22:23], 0, s[22:23]
	s_waitcnt lgkmcnt(0)
	v_add_f32_e32 v20, v20, v21
	global_store_dword v[22:23], v20, off
.LBB0_2151:
	s_or_b64 exec, exec, s[20:21]
	v_add_u32_e32 v20, 0xb0, v144
	s_waitcnt lgkmcnt(0)
	v_ashrrev_i32_e32 v21, 31, v20
	v_lshlrev_b64 v[22:23], 11, v[20:21]
	v_lshl_add_u64 v[22:23], s[4:5], 0, v[22:23]
	v_lshl_add_u64 v[22:23], s[18:19], 1, v[22:23]
	v_lshl_add_u64 v[22:23], v[22:23], 0, s[50:51]
	v_lshl_add_u64 v[22:23], v[22:23], 0, v[2:3]
	v_mov_b32_e32 v24, v244
	v_mov_b32_e32 v25, v245
	v_mov_b32_e32 v26, v246
	v_mov_b32_e32 v27, v247
	v_lshlrev_b32_e32 v28, 16, v24
	v_and_b32_e32 v29, 0xffff0000, v24
	v_lshlrev_b32_e32 v24, 16, v25
	v_and_b32_e32 v25, 0xffff0000, v25
	v_pk_add_f32 v[18:19], v[18:19], v[24:25]
	v_lshlrev_b32_e32 v24, 16, v26
	v_and_b32_e32 v25, 0xffff0000, v26
	v_lshlrev_b32_e32 v26, 16, v27
	v_and_b32_e32 v27, 0xffff0000, v27
	v_pk_add_f32 v[16:17], v[16:17], v[28:29]
	v_pk_add_f32 v[26:27], v[14:15], v[26:27]
	v_pk_add_f32 v[24:25], v[12:13], v[24:25]
	v_cvt_pk_bf16_f32 v12, v16, v17
	v_cvt_pk_bf16_f32 v13, v18, v19
	v_cvt_pk_bf16_f32 v14, v24, v25
	v_cvt_pk_bf16_f32 v15, v26, v27
	global_store_dwordx4 v[22:23], v[12:15], off
	v_mul_f32_e32 v2, v17, v17
	v_fmac_f32_e32 v2, v16, v16
	v_mul_f32_e32 v12, v19, v19
	v_fmac_f32_e32 v12, v18, v18
	v_add_f32_e32 v2, v2, v12
	v_mul_f32_e32 v12, v25, v25
	v_fmac_f32_e32 v12, v24, v24
	v_add_f32_e32 v2, v12, v2
	v_mul_f32_e32 v12, v27, v27
	v_fmac_f32_e32 v12, v26, v26
	v_add_f32_e32 v2, v12, v2
	v_mov_b32_e32 v12, v248
	v_mov_b32_e32 v13, v249
	v_mov_b32_e32 v14, v250
	v_mov_b32_e32 v15, v251
	v_lshlrev_b32_e32 v16, 16, v12
	v_and_b32_e32 v17, 0xffff0000, v12
	v_lshlrev_b32_e32 v12, 16, v13
	v_and_b32_e32 v13, 0xffff0000, v13
	v_pk_add_f32 v[10:11], v[10:11], v[12:13]
	v_lshlrev_b32_e32 v12, 16, v14
	v_and_b32_e32 v13, 0xffff0000, v14
	v_lshlrev_b32_e32 v14, 16, v15
	v_and_b32_e32 v15, 0xffff0000, v15
	v_pk_add_f32 v[8:9], v[8:9], v[16:17]
	v_pk_add_f32 v[14:15], v[6:7], v[14:15]
	v_pk_add_f32 v[12:13], v[4:5], v[12:13]
	v_cvt_pk_bf16_f32 v4, v8, v9
	v_cvt_pk_bf16_f32 v5, v10, v11
	v_cvt_pk_bf16_f32 v6, v12, v13
	v_cvt_pk_bf16_f32 v7, v14, v15
	global_store_dwordx4 v[22:23], v[4:7], off offset:256
	s_nop 1
	v_mul_f32_e32 v4, v9, v9
	v_mul_f32_e32 v5, v11, v11
	v_fmac_f32_e32 v4, v8, v8
	v_fmac_f32_e32 v5, v10, v10
	v_add_f32_e32 v4, v4, v5
	v_mul_f32_e32 v5, v13, v13
	v_fmac_f32_e32 v5, v12, v12
	v_add_f32_e32 v4, v5, v4
	v_mul_f32_e32 v5, v15, v15
	v_fmac_f32_e32 v5, v14, v14
	v_add_f32_e32 v4, v5, v4
	v_add_f32_e32 v2, v2, v4
	ds_bpermute_b32 v4, v152, v2
	s_waitcnt lgkmcnt(0)
	v_add_f32_e32 v2, v2, v4
	ds_bpermute_b32 v4, v151, v2
	s_and_saveexec_b64 s[18:19], vcc
	s_cbranch_execz .LBB0_2130
	v_lshlrev_b64 v[6:7], 6, v[20:21]
	v_lshl_add_u64 v[6:7], s[2:3], 0, v[6:7]
	v_lshl_add_u64 v[6:7], s[16:17], 2, v[6:7]
	s_lshl_b32 s16, s36, 2
	s_mov_b32 s17, s51
	v_lshl_add_u64 v[6:7], v[6:7], 0, s[16:17]
	s_waitcnt lgkmcnt(0)
	v_add_f32_e32 v2, v2, v4
	global_store_dword v[6:7], v2, off
	s_branch .LBB0_2130
